# strategy 6.4/7.2 (lead the compute segment with resident data): attention tile loop issues the first six K-fragment ds_reads right after the barrier and the next tile's LDS-DMA issue block behind them
# speedup vs baseline: 1.0063x; 1.0063x over previous
.Lprio_skip_a1:
.LBB0_805:
	s_add_i32 s56, s12, -1
	s_waitcnt vmcnt(0)
	s_and_b32 s87, s56, 1
	s_cmp_ge_u32 s12, s85
	s_waitcnt vmcnt(0) lgkmcnt(0)
	s_barrier


.LBB0_807:
	s_mul_i32 s56, s87, 0x6000
	s_add_i32 s56, s56, 0
	s_add_i32 s56, s56, 0x8000
	v_add_u32_e32 v175, s56, v161
	ds_read_b128 v[66:69], v175 offset:0
	ds_read_b128 v[70:73], v175 offset:0x3000
	v_add_u32_e32 v200, s56, v169
	ds_read_b128 v[176:179], v200 offset:0
	ds_read_b128 v[180:183], v200 offset:0x3000
	v_add_u32_e32 v201, s56, v170
	ds_read_b128 v[184:187], v201 offset:0
	ds_read_b128 v[188:191], v201 offset:0x3000
	s_cmp_ge_u32 s12, s85
	s_cbranch_scc1 .Ldma_skip_a1
	s_xor_b32 s88, s87, 1
	s_mulk_i32 s88, 0x6000
	s_add_i32 s88, s64, s88
	s_add_i32 m0, s88, 0x8000
	s_nop 0
	global_load_lds_dwordx4 v244, s[94:95]
	s_add_i32 m0, s88, 0xa000
	s_nop 0
	global_load_lds_dwordx4 v243, s[94:95]
	s_add_i32 m0, s88, 0xc000
	s_lshl_b32 s88, s87, 14
	s_xor_b32 s88, s88, 0x4000
	s_add_i32 s88, s64, s88
	global_load_lds_dwordx4 v242, s[94:95]
	s_mov_b32 m0, s88
	s_nop 0
	global_load_lds_dwordx4 v241, s[96:97]
	s_add_i32 m0, s88, 0x2000
	s_nop 0
	global_load_lds_dwordx4 v240, s[96:97]
.Ldma_skip_a1:
	s_waitcnt lgkmcnt(4)
	v_add_u32_e32 v202, s56, v171
	v_mfma_f32_32x32x16_bf16 v[82:97], v[66:69], v[98:101], v[206:221]
	ds_read_b128 v[192:195], v202 offset:0
	ds_read_b128 v[196:199], v202 offset:0x3000
	s_waitcnt lgkmcnt(4)
	v_mfma_f32_32x32x16_bf16 v[66:81], v[70:73], v[98:101], v[206:221]
	v_mfma_f32_32x32x16_bf16 v[82:97], v[176:179], v[102:105], v[82:97]
	ds_read_b128 v[176:179], v175 offset:0x80
	v_mfma_f32_32x32x16_bf16 v[66:81], v[180:183], v[102:105], v[66:81]
	ds_read_b128 v[180:183], v175 offset:0x3080
	s_waitcnt lgkmcnt(4)
	v_mfma_f32_32x32x16_bf16 v[82:97], v[184:187], v[106:109], v[82:97]
	ds_read_b128 v[184:187], v200 offset:0x80
	v_mfma_f32_32x32x16_bf16 v[66:81], v[188:191], v[106:109], v[66:81]
	ds_read_b128 v[188:191], v200 offset:0x3080
	s_waitcnt lgkmcnt(4)
	v_mfma_f32_32x32x16_bf16 v[82:97], v[192:195], v[110:113], v[82:97]
	ds_read_b128 v[192:195], v201 offset:0x80
	v_mfma_f32_32x32x16_bf16 v[66:81], v[196:199], v[110:113], v[66:81]
	ds_read_b128 v[196:199], v201 offset:0x3080
	s_waitcnt lgkmcnt(4)
	v_mfma_f32_32x32x16_bf16 v[82:97], v[176:179], v[114:117], v[82:97]
	ds_read_b128 v[176:179], v202 offset:0x80
	v_mfma_f32_32x32x16_bf16 v[66:81], v[180:183], v[114:117], v[66:81]
	ds_read_b128 v[180:183], v202 offset:0x3080
	s_waitcnt lgkmcnt(4)
	v_mfma_f32_32x32x16_bf16 v[82:97], v[184:187], v[118:121], v[82:97]
	ds_read_b128 v[184:187], v175 offset:0x100
	v_mfma_f32_32x32x16_bf16 v[66:81], v[188:191], v[118:121], v[66:81]
	ds_read_b128 v[188:191], v175 offset:0x3100
	s_waitcnt lgkmcnt(4)
	v_mfma_f32_32x32x16_bf16 v[82:97], v[192:195], v[122:125], v[82:97]
	ds_read_b128 v[192:195], v200 offset:0x100
	v_mfma_f32_32x32x16_bf16 v[66:81], v[196:199], v[122:125], v[66:81]
	ds_read_b128 v[196:199], v200 offset:0x3100
	s_waitcnt lgkmcnt(4)
	v_mfma_f32_32x32x16_bf16 v[82:97], v[176:179], v[126:129], v[82:97]
	ds_read_b128 v[176:179], v201 offset:0x100
	v_mfma_f32_32x32x16_bf16 v[66:81], v[180:183], v[126:129], v[66:81]
	ds_read_b128 v[180:183], v201 offset:0x3100
	s_waitcnt lgkmcnt(4)
	v_mfma_f32_32x32x16_bf16 v[82:97], v[184:187], v[130:133], v[82:97]
	ds_read_b128 v[184:187], v202 offset:0x100
	v_mfma_f32_32x32x16_bf16 v[66:81], v[188:191], v[130:133], v[66:81]
	ds_read_b128 v[188:191], v202 offset:0x3100
	s_waitcnt lgkmcnt(4)
	v_mfma_f32_32x32x16_bf16 v[82:97], v[192:195], v[134:137], v[82:97]
	s_waitcnt lgkmcnt(2)
	v_mfma_f32_32x32x16_bf16 v[66:81], v[196:199], v[134:137], v[66:81]
	v_mfma_f32_32x32x16_bf16 v[82:97], v[176:179], v[138:141], v[82:97]
	s_waitcnt lgkmcnt(0)
	v_mfma_f32_32x32x16_bf16 v[66:81], v[180:183], v[138:141], v[66:81]
	v_mfma_f32_32x32x16_bf16 v[82:97], v[184:187], v[142:145], v[82:97]
	s_add_i32 s56, s86, 0x13f
	s_cmp_le_i32 s56, s84
	v_mfma_f32_32x32x16_bf16 v[66:81], v[188:191], v[142:145], v[66:81]
	s_cbranch_scc1 .LBB0_809
	v_add_u32_e32 v175, s83, v168
	v_cmp_lt_i32_e32 vcc, -1, v175
	v_add_u32_e32 v176, -1, v175
	s_nop 4
	v_cndmask_b32_e32 v82, v165, v82, vcc
	v_cmp_lt_i32_e32 vcc, 31, v175
	s_nop 1
	v_cndmask_b32_e32 v66, v165, v66, vcc
	v_cmp_lt_i32_e32 vcc, -1, v176
	s_nop 1
	v_cndmask_b32_e32 v83, v165, v83, vcc
	v_cmp_lt_i32_e32 vcc, 31, v176
	v_add_u32_e32 v176, -2, v175
	s_nop 0
	v_cndmask_b32_e32 v67, v165, v67, vcc
	v_cmp_lt_i32_e32 vcc, -1, v176
	s_nop 1
	v_cndmask_b32_e32 v84, v165, v84, vcc
	v_cmp_lt_i32_e32 vcc, 31, v176
	v_add_u32_e32 v176, -3, v175
	s_nop 0
	v_cndmask_b32_e32 v68, v165, v68, vcc
	v_cmp_lt_i32_e32 vcc, -1, v176
	s_nop 1
	v_cndmask_b32_e32 v85, v165, v85, vcc
	v_cmp_lt_i32_e32 vcc, 31, v176
	v_add_u32_e32 v176, -4, v175
	s_nop 0
	v_cndmask_b32_e32 v69, v165, v69, vcc
	v_cmp_lt_i32_e32 vcc, -1, v176
	s_nop 1
	v_cndmask_b32_e32 v86, v165, v86, vcc
	v_cmp_lt_i32_e32 vcc, 31, v176
	v_add_u32_e32 v176, -5, v175
	s_nop 0
	v_cndmask_b32_e32 v70, v165, v70, vcc
	v_cmp_lt_i32_e32 vcc, -1, v176
	s_nop 1
	v_cndmask_b32_e32 v87, v165, v87, vcc
	v_cmp_lt_i32_e32 vcc, 31, v176
	v_add_u32_e32 v176, -6, v175
	s_nop 0
	v_cndmask_b32_e32 v71, v165, v71, vcc
	v_cmp_lt_i32_e32 vcc, -1, v176
	s_nop 1
	v_cndmask_b32_e32 v88, v165, v88, vcc
	v_cmp_lt_i32_e32 vcc, 31, v176
	v_add_u32_e32 v176, -7, v175
	s_nop 0
	v_cndmask_b32_e32 v72, v165, v72, vcc
	v_cmp_lt_i32_e32 vcc, -1, v176
	s_nop 1
	v_cndmask_b32_e32 v89, v165, v89, vcc
	v_cmp_lt_i32_e32 vcc, 31, v176
	v_add_u32_e32 v176, -16, v175
	s_nop 0
	v_cndmask_b32_e32 v73, v165, v73, vcc
	v_cmp_lt_i32_e32 vcc, -1, v176
	s_nop 1
	v_cndmask_b32_e32 v90, v165, v90, vcc
	v_cmp_lt_i32_e32 vcc, 31, v176
	v_subrev_u32_e32 v176, 17, v175
	s_nop 0
	v_cndmask_b32_e32 v74, v165, v74, vcc
	v_cmp_lt_i32_e32 vcc, -1, v176
	s_nop 1
	v_cndmask_b32_e32 v91, v165, v91, vcc
	v_cmp_lt_i32_e32 vcc, 31, v176
	v_subrev_u32_e32 v176, 18, v175
	s_nop 0
	v_cndmask_b32_e32 v75, v165, v75, vcc
	v_cmp_lt_i32_e32 vcc, -1, v176
	s_nop 1
	v_cndmask_b32_e32 v92, v165, v92, vcc
	v_cmp_lt_i32_e32 vcc, 31, v176
	v_subrev_u32_e32 v176, 19, v175
	s_nop 0
	v_cndmask_b32_e32 v76, v165, v76, vcc
	v_cmp_lt_i32_e32 vcc, -1, v176
	s_nop 1
	v_cndmask_b32_e32 v93, v165, v93, vcc
	v_cmp_lt_i32_e32 vcc, 31, v176
	v_subrev_u32_e32 v176, 20, v175
	s_nop 0
	v_cndmask_b32_e32 v77, v165, v77, vcc
	v_cmp_lt_i32_e32 vcc, -1, v176
	s_nop 1
	v_cndmask_b32_e32 v94, v165, v94, vcc
	v_cmp_lt_i32_e32 vcc, 31, v176
	v_subrev_u32_e32 v176, 21, v175
	s_nop 0
	v_cndmask_b32_e32 v78, v165, v78, vcc
	v_cmp_lt_i32_e32 vcc, -1, v176
	s_nop 1
	v_cndmask_b32_e32 v95, v165, v95, vcc
	v_cmp_lt_i32_e32 vcc, 31, v176
	v_subrev_u32_e32 v176, 22, v175
	v_subrev_u32_e32 v175, 23, v175
	v_cndmask_b32_e32 v79, v165, v79, vcc
	v_cmp_lt_i32_e32 vcc, -1, v176
	s_nop 1
	v_cndmask_b32_e32 v96, v165, v96, vcc
	v_cmp_lt_i32_e32 vcc, 31, v176
	s_nop 1
	v_cndmask_b32_e32 v80, v165, v80, vcc
	v_cmp_lt_i32_e32 vcc, -1, v175
	s_nop 1
	v_cndmask_b32_e32 v97, v165, v97, vcc
	v_cmp_lt_i32_e32 vcc, 31, v175
	s_nop 1
	v_cndmask_b32_e32 v81, v165, v81, vcc

.Lprio_skip_a2:
.LBB0_946:
	s_add_i32 s44, s12, -1
	s_waitcnt vmcnt(0)
	s_and_b32 s48, s44, 1
	s_cmp_ge_u32 s12, s46
	s_waitcnt vmcnt(0) lgkmcnt(0)
	s_barrier


.LBB0_948:
	s_mul_i32 s44, s48, 0x6000
	s_add_i32 s44, s44, 0
	s_add_i32 s44, s44, 0x8000
	v_add_u32_e32 v177, s44, v171
	ds_read_b128 v[66:69], v177 offset:0
	ds_read_b128 v[82:85], v177 offset:0x3000
	v_add_u32_e32 v206, s44, v172
	ds_read_b128 v[178:181], v206 offset:0
	ds_read_b128 v[182:185], v206 offset:0x3000
	v_add_u32_e32 v207, s44, v173
	ds_read_b128 v[186:189], v207 offset:0
	ds_read_b128 v[190:193], v207 offset:0x3000
	s_cmp_ge_u32 s12, s46
	s_cbranch_scc1 .Ldma_skip_a2
	s_xor_b32 s88, s48, 1
	s_mulk_i32 s88, 0x6000
	s_add_i32 s88, s64, s88
	s_add_i32 m0, s88, 0x8000
	s_nop 0
	global_load_lds_dwordx4 v244, s[94:95]
	s_add_i32 m0, s88, 0xa000
	s_nop 0
	global_load_lds_dwordx4 v243, s[94:95]
	s_add_i32 m0, s88, 0xc000
	s_lshl_b32 s88, s48, 14
	s_xor_b32 s88, s88, 0x4000
	s_add_i32 s88, s64, s88
	global_load_lds_dwordx4 v242, s[94:95]
	s_mov_b32 m0, s88
	s_nop 0
	global_load_lds_dwordx4 v241, s[96:97]
	s_add_i32 m0, s88, 0x2000
	s_nop 0
	global_load_lds_dwordx4 v240, s[96:97]
.Ldma_skip_a2:
	s_waitcnt lgkmcnt(4)
	v_add_u32_e32 v208, s44, v174
	v_mfma_f32_32x32x16_bf16 v[66:81], v[66:69], v[98:101], v[210:225]
	ds_read_b128 v[194:197], v208 offset:0
	ds_read_b128 v[198:201], v208 offset:0x3000
	s_waitcnt lgkmcnt(4)
	v_mfma_f32_32x32x16_bf16 v[82:97], v[82:85], v[98:101], v[210:225]
	v_mfma_f32_32x32x16_bf16 v[66:81], v[178:181], v[102:105], v[66:81]
	ds_read_b128 v[178:181], v177 offset:0x80
	ds_read_b128 v[202:205], v177 offset:0x3080
	s_waitcnt lgkmcnt(4)
	v_mfma_f32_32x32x16_bf16 v[82:97], v[182:185], v[102:105], v[82:97]
	v_mfma_f32_32x32x16_bf16 v[66:81], v[186:189], v[106:109], v[66:81]
	ds_read_b128 v[182:185], v206 offset:0x80
	ds_read_b128 v[186:189], v206 offset:0x3080
	s_waitcnt lgkmcnt(4)
	v_mfma_f32_32x32x16_bf16 v[82:97], v[190:193], v[106:109], v[82:97]
	v_mfma_f32_32x32x16_bf16 v[66:81], v[194:197], v[110:113], v[66:81]
	ds_read_b128 v[190:193], v207 offset:0x80
	ds_read_b128 v[194:197], v207 offset:0x3080
	s_waitcnt lgkmcnt(4)
	v_mfma_f32_32x32x16_bf16 v[82:97], v[198:201], v[110:113], v[82:97]
	v_mfma_f32_32x32x16_bf16 v[66:81], v[178:181], v[114:117], v[66:81]
	ds_read_b128 v[178:181], v208 offset:0x80
	ds_read_b128 v[198:201], v208 offset:0x3080
	s_waitcnt lgkmcnt(4)
	v_mfma_f32_32x32x16_bf16 v[82:97], v[202:205], v[114:117], v[82:97]
	v_mfma_f32_32x32x16_bf16 v[66:81], v[182:185], v[118:121], v[66:81]
	ds_read_b128 v[182:185], v177 offset:0x100
	ds_read_b128 v[202:205], v177 offset:0x3100
	s_waitcnt lgkmcnt(4)
	v_mfma_f32_32x32x16_bf16 v[82:97], v[186:189], v[118:121], v[82:97]
	v_mfma_f32_32x32x16_bf16 v[66:81], v[190:193], v[122:125], v[66:81]
	ds_read_b128 v[186:189], v206 offset:0x100
	ds_read_b128 v[190:193], v206 offset:0x3100
	s_waitcnt lgkmcnt(4)
	v_mfma_f32_32x32x16_bf16 v[82:97], v[194:197], v[122:125], v[82:97]
	v_mfma_f32_32x32x16_bf16 v[66:81], v[178:181], v[126:129], v[66:81]
	ds_read_b128 v[178:181], v207 offset:0x100
	ds_read_b128 v[194:197], v207 offset:0x3100
	s_waitcnt lgkmcnt(4)
	v_mfma_f32_32x32x16_bf16 v[82:97], v[198:201], v[126:129], v[82:97]
	v_mfma_f32_32x32x16_bf16 v[66:81], v[182:185], v[130:133], v[66:81]
	ds_read_b128 v[182:185], v208 offset:0x100
	ds_read_b128 v[198:201], v208 offset:0x3100
	s_waitcnt lgkmcnt(4)
	v_mfma_f32_32x32x16_bf16 v[82:97], v[202:205], v[130:133], v[82:97]
	v_mfma_f32_32x32x16_bf16 v[66:81], v[186:189], v[134:137], v[66:81]
	s_waitcnt lgkmcnt(2)
	v_mfma_f32_32x32x16_bf16 v[82:97], v[190:193], v[134:137], v[82:97]
	v_mfma_f32_32x32x16_bf16 v[66:81], v[178:181], v[138:141], v[66:81]
	s_waitcnt lgkmcnt(0)
	v_mfma_f32_32x32x16_bf16 v[82:97], v[194:197], v[138:141], v[82:97]
	v_mfma_f32_32x32x16_bf16 v[66:81], v[182:185], v[142:145], v[66:81]
	s_add_i32 s44, s47, 0x13f
	s_cmp_le_i32 s44, s55
	v_mfma_f32_32x32x16_bf16 v[82:97], v[198:201], v[142:145], v[82:97]
	s_cbranch_scc1 .LBB0_950
	v_add_u32_e32 v177, s54, v167
	v_cmp_lt_i32_e32 vcc, -1, v177
	v_add_u32_e32 v178, -1, v177
	s_nop 4
	v_cndmask_b32_e32 v66, v165, v66, vcc
	v_cmp_lt_i32_e32 vcc, 31, v177
	s_nop 1
	v_cndmask_b32_e32 v82, v165, v82, vcc
	v_cmp_lt_i32_e32 vcc, -1, v178
	s_nop 1
	v_cndmask_b32_e32 v67, v165, v67, vcc
	v_cmp_lt_i32_e32 vcc, 31, v178
	v_add_u32_e32 v178, -2, v177
	s_nop 0
	v_cndmask_b32_e32 v83, v165, v83, vcc
	v_cmp_lt_i32_e32 vcc, -1, v178
	s_nop 1
	v_cndmask_b32_e32 v68, v165, v68, vcc
	v_cmp_lt_i32_e32 vcc, 31, v178
	v_add_u32_e32 v178, -3, v177
	s_nop 0
	v_cndmask_b32_e32 v84, v165, v84, vcc
	v_cmp_lt_i32_e32 vcc, -1, v178
	s_nop 1
	v_cndmask_b32_e32 v69, v165, v69, vcc
	v_cmp_lt_i32_e32 vcc, 31, v178
	v_add_u32_e32 v178, -4, v177
	s_nop 0
	v_cndmask_b32_e32 v85, v165, v85, vcc
	v_cmp_lt_i32_e32 vcc, -1, v178
	s_nop 1
	v_cndmask_b32_e32 v70, v165, v70, vcc
	v_cmp_lt_i32_e32 vcc, 31, v178
	v_add_u32_e32 v178, -5, v177
	s_nop 0
	v_cndmask_b32_e32 v86, v165, v86, vcc
	v_cmp_lt_i32_e32 vcc, -1, v178
	s_nop 1
	v_cndmask_b32_e32 v71, v165, v71, vcc
	v_cmp_lt_i32_e32 vcc, 31, v178
	v_add_u32_e32 v178, -6, v177
	s_nop 0
	v_cndmask_b32_e32 v87, v165, v87, vcc
	v_cmp_lt_i32_e32 vcc, -1, v178
	s_nop 1
	v_cndmask_b32_e32 v72, v165, v72, vcc
	v_cmp_lt_i32_e32 vcc, 31, v178
	v_add_u32_e32 v178, -7, v177
	s_nop 0
	v_cndmask_b32_e32 v88, v165, v88, vcc
	v_cmp_lt_i32_e32 vcc, -1, v178
	s_nop 1
	v_cndmask_b32_e32 v73, v165, v73, vcc
	v_cmp_lt_i32_e32 vcc, 31, v178
	v_add_u32_e32 v178, -16, v177
	s_nop 0
	v_cndmask_b32_e32 v89, v165, v89, vcc
	v_cmp_lt_i32_e32 vcc, -1, v178
	s_nop 1
	v_cndmask_b32_e32 v74, v165, v74, vcc
	v_cmp_lt_i32_e32 vcc, 31, v178
	v_subrev_u32_e32 v178, 17, v177
	s_nop 0
	v_cndmask_b32_e32 v90, v165, v90, vcc
	v_cmp_lt_i32_e32 vcc, -1, v178
	s_nop 1
	v_cndmask_b32_e32 v75, v165, v75, vcc
	v_cmp_lt_i32_e32 vcc, 31, v178
	v_subrev_u32_e32 v178, 18, v177
	s_nop 0
	v_cndmask_b32_e32 v91, v165, v91, vcc
	v_cmp_lt_i32_e32 vcc, -1, v178
	s_nop 1
	v_cndmask_b32_e32 v76, v165, v76, vcc
	v_cmp_lt_i32_e32 vcc, 31, v178
	v_subrev_u32_e32 v178, 19, v177
	s_nop 0
	v_cndmask_b32_e32 v92, v165, v92, vcc
	v_cmp_lt_i32_e32 vcc, -1, v178
	s_nop 1
	v_cndmask_b32_e32 v77, v165, v77, vcc
	v_cmp_lt_i32_e32 vcc, 31, v178
	v_subrev_u32_e32 v178, 20, v177
	s_nop 0
	v_cndmask_b32_e32 v93, v165, v93, vcc
	v_cmp_lt_i32_e32 vcc, -1, v178
	s_nop 1
	v_cndmask_b32_e32 v78, v165, v78, vcc
	v_cmp_lt_i32_e32 vcc, 31, v178
	v_subrev_u32_e32 v178, 21, v177
	s_nop 0
	v_cndmask_b32_e32 v94, v165, v94, vcc
	v_cmp_lt_i32_e32 vcc, -1, v178
	s_nop 1
	v_cndmask_b32_e32 v79, v165, v79, vcc
	v_cmp_lt_i32_e32 vcc, 31, v178
	v_subrev_u32_e32 v178, 22, v177
	v_subrev_u32_e32 v177, 23, v177
	v_cndmask_b32_e32 v95, v165, v95, vcc
	v_cmp_lt_i32_e32 vcc, -1, v178
	s_nop 1
	v_cndmask_b32_e32 v80, v165, v80, vcc
	v_cmp_lt_i32_e32 vcc, 31, v178
	s_nop 1
	v_cndmask_b32_e32 v96, v165, v96, vcc
	v_cmp_lt_i32_e32 vcc, -1, v177
	s_nop 1
	v_cndmask_b32_e32 v81, v165, v81, vcc
	v_cmp_lt_i32_e32 vcc, 31, v177
	s_nop 1
	v_cndmask_b32_e32 v97, v165, v97, vcc
